# Final combine+RMSNorm loop: the 40 row loads issued up front (30 together, 10 as soon as registers free) with counted waits; was one round trip per 512-byte column group
# speedup vs baseline: 1.0306x; 1.0094x over previous
; __global__ void __launch_bounds__(NWAVES * 64, 2) trunk_fwd(Args args) {
;     ...
;                 for (int m = gw; m < M; m += ngw) {
;                     const int p0 = TOKP[2 * m], p1 = TOKP[2 * m + 1]; const float g0 = TOKW[2 * m], g1 = TOKW[2 * m + 1];
;                     const f32x4* xr = (const f32x4*)(XA + (size_t)m * D) + lane; const v2u* y0 = (const v2u*)(YPERM + (size_t)p0 * D) + lane; const v2u* y1 = (const v2u*)(YPERM + (size_t)p1 * D) + lane;
;                     const v2u* z0 = (const v2u*)(HPERM + (size_t)p0 * D) + lane; const v2u* z1 = (const v2u*)(HPERM + (size_t)p1 * D) + lane;
;                     f32x4 v[8]; float s = 0.f;
; #pragma unroll
;                     for (int jj = 0; jj < 8; ++jj) { const v2u a = y0[64 * jj], c = y1[64 * jj], a2 = z0[64 * jj], c2 = z1[64 * jj]; f32x4 x = xr[64 * jj];
;                         x.x += g0 * (bflo(a.x) + bflo(a2.x)) + g1 * (bflo(c.x) + bflo(c2.x)); x.y += g0 * (bfhi(a.x) + bfhi(a2.x)) + g1 * (bfhi(c.x) + bfhi(c2.x));
;                         x.z += g0 * (bflo(a.y) + bflo(a2.y)) + g1 * (bflo(c.y) + bflo(c2.y)); x.w += g0 * (bfhi(a.y) + bfhi(a2.y)) + g1 * (bfhi(c.y) + bfhi(c2.y));
;                         v[jj] = x; s += (x.x * x.x + x.y * x.y) + (x.z * x.z + x.w * x.w); }
.LBB0_1349:
	s_ashr_i32 s11, s10, 31
	s_lshl_b64 s[4:5], s[10:11], 2
	s_add_u32 s14, s18, s4
	s_addc_u32 s15, s19, s5
	global_load_dwordx2 v[2:3], v187, s[14:15]
	s_add_i32 s14, s10, 1
	s_ashr_i32 s15, s14, 31
	s_add_u32 s4, s23, s4
	s_addc_u32 s5, s17, s5
	global_load_dword v52, v187, s[4:5]
	s_lshl_b64 s[4:5], s[14:15], 2
	s_add_u32 s4, s23, s4
	s_addc_u32 s5, s17, s5
	global_load_dword v53, v187, s[4:5]
	v_lshl_add_u64 v[4:5], s[12:13], 0, v[186:187]
	s_mov_b32 s4, 0x36da1000
	s_add_i32 s7, s7, s16
	s_waitcnt vmcnt(0)
	v_ashrrev_i32_e32 v7, 31, v2
	v_mov_b32_e32 v6, v2
	v_lshlrev_b64 v[6:7], 12, v[6:7]
	v_lshl_add_u64 v[18:19], v[28:29], 0, v[6:7]
	v_lshl_add_u64 v[76:77], v[30:31], 0, v[6:7]
	v_add_co_u32_e32 v6, vcc, s4, v4
	v_ashrrev_i32_e32 v9, 31, v3
	s_nop 0
	v_addc_co_u32_e32 v7, vcc, 0, v5, vcc
	v_mov_b32_e32 v8, v3
	v_add_co_u32_e32 v96, vcc, s28, v4
	v_lshlrev_b64 v[2:3], 12, v[8:9]
	s_nop 0
	v_addc_co_u32_e32 v97, vcc, 0, v5, vcc
	v_lshl_add_u64 v[68:69], v[28:29], 0, v[2:3]
	v_lshl_add_u64 v[92:93], v[30:31], 0, v[2:3]
	global_load_dwordx2 v[122:123], v[18:19], off
	global_load_dwordx2 v[156:157], v[68:69], off
	global_load_dwordx2 v[158:159], v[76:77], off
	global_load_dwordx2 v[160:161], v[92:93], off
	global_load_dwordx4 v[162:165], v[96:97], off offset:-4096
	global_load_dwordx2 v[166:167], v[18:19], off offset:512
	global_load_dwordx2 v[168:169], v[68:69], off offset:512
	global_load_dwordx2 v[170:171], v[76:77], off offset:512
	global_load_dwordx2 v[172:173], v[92:93], off offset:512
	global_load_dwordx4 v[174:177], v[6:7], off offset:1024
	global_load_dwordx2 v[178:179], v[18:19], off offset:1024
	global_load_dwordx2 v[180:181], v[68:69], off offset:1024
	global_load_dwordx2 v[182:183], v[76:77], off offset:1024
	global_load_dwordx2 v[184:185], v[92:93], off offset:1024
	global_load_dwordx4 v[200:203], v[6:7], off offset:2048
	global_load_dwordx2 v[204:205], v[18:19], off offset:1536
	global_load_dwordx2 v[206:207], v[68:69], off offset:1536
	global_load_dwordx2 v[208:209], v[76:77], off offset:1536
	global_load_dwordx2 v[210:211], v[92:93], off offset:1536
	global_load_dwordx4 v[212:215], v[6:7], off offset:3072
	global_load_dwordx2 v[216:217], v[18:19], off offset:2048
	global_load_dwordx2 v[218:219], v[68:69], off offset:2048
	global_load_dwordx2 v[220:221], v[76:77], off offset:2048
	global_load_dwordx2 v[222:223], v[92:93], off offset:2048
	global_load_dwordx4 v[232:235], v[96:97], off
	global_load_dwordx2 v[236:237], v[18:19], off offset:2560
	global_load_dwordx2 v[238:239], v[68:69], off offset:2560
	global_load_dwordx2 v[240:241], v[76:77], off offset:2560
	global_load_dwordx2 v[242:243], v[92:93], off offset:2560
	global_load_dwordx4 v[244:247], v[96:97], off offset:1024
	v_mov_b32_e32 v94, v53
	s_waitcnt vmcnt(24)
	v_lshlrev_b32_e32 v16, 16, v166
	s_waitcnt vmcnt(23)
	v_lshlrev_b32_e32 v17, 16, v168
	s_waitcnt vmcnt(22)
	v_lshlrev_b32_e32 v20, 16, v170
	s_waitcnt vmcnt(21)
	v_lshlrev_b32_e32 v21, 16, v172
	v_pk_add_f32 v[16:17], v[16:17], v[20:21]
	v_and_b32_e32 v21, 0xffff0000, v172
	v_pk_mul_f32 v[64:65], v[52:53], v[16:17]
	v_and_b32_e32 v17, 0xffff0000, v168
	v_and_b32_e32 v16, 0xffff0000, v166
	v_and_b32_e32 v20, 0xffff0000, v170
	v_pk_add_f32 v[16:17], v[16:17], v[20:21]
	v_lshlrev_b32_e32 v21, 16, v173
	v_pk_mul_f32 v[66:67], v[52:53], v[16:17]
	v_lshlrev_b32_e32 v17, 16, v169
	v_lshlrev_b32_e32 v16, 16, v167
	v_lshlrev_b32_e32 v20, 16, v171
	v_and_b32_e32 v169, 0xffff0000, v169
	v_and_b32_e32 v168, 0xffff0000, v167
	v_and_b32_e32 v167, 0xffff0000, v173
	v_and_b32_e32 v166, 0xffff0000, v171
	v_pk_add_f32 v[16:17], v[16:17], v[20:21]
	v_pk_add_f32 v[2:3], v[168:169], v[166:167]
	v_pk_mul_f32 v[54:55], v[52:53], v[16:17]
	v_pk_mul_f32 v[56:57], v[52:53], v[2:3]
	v_lshlrev_b32_e32 v120, 16, v160
	v_and_b32_e32 v121, 0xffff0000, v160
	v_lshlrev_b32_e32 v160, 16, v161
	v_and_b32_e32 v161, 0xffff0000, v161
	s_waitcnt vmcnt(19)
	v_lshlrev_b32_e32 v23, 16, v179
	v_lshlrev_b32_e32 v22, 16, v178
	s_waitcnt vmcnt(17)
	v_lshlrev_b32_e32 v43, 16, v183
	v_lshlrev_b32_e32 v42, 16, v182
	v_and_b32_e32 v179, 0xffff0000, v179
	v_and_b32_e32 v178, 0xffff0000, v178
	v_and_b32_e32 v183, 0xffff0000, v183
	v_and_b32_e32 v182, 0xffff0000, v182
	v_pk_add_f32 v[22:23], v[22:23], v[42:43]
	v_lshlrev_b32_e32 v43, 16, v181
	v_lshlrev_b32_e32 v42, 16, v180
	s_waitcnt vmcnt(16)
	v_lshlrev_b32_e32 v45, 16, v185
	v_lshlrev_b32_e32 v44, 16, v184
	v_pk_add_f32 v[8:9], v[178:179], v[182:183]
	v_and_b32_e32 v181, 0xffff0000, v181
	v_and_b32_e32 v180, 0xffff0000, v180
	v_and_b32_e32 v183, 0xffff0000, v185
	v_and_b32_e32 v182, 0xffff0000, v184
	v_pk_add_f32 v[42:43], v[42:43], v[44:45]
	v_pk_add_f32 v[14:15], v[180:181], v[182:183]
	v_pk_mul_f32 v[42:43], v[94:95], v[42:43] op_sel_hi:[0,1]
	v_pk_mul_f32 v[14:15], v[94:95], v[14:15] op_sel_hi:[0,1]
	v_pk_fma_f32 v[22:23], v[52:53], v[22:23], v[42:43] op_sel_hi:[0,1,1]
	s_waitcnt vmcnt(15)
	v_mov_b32_e32 v42, v200
	v_mov_b32_e32 v43, v202
	v_pk_fma_f32 v[8:9], v[52:53], v[8:9], v[14:15] op_sel_hi:[0,1,1]
	v_mov_b32_e32 v202, v201
	v_pk_add_f32 v[58:59], v[42:43], v[22:23]
	v_pk_add_f32 v[42:43], v[202:203], v[8:9]
	global_load_dwordx2 v[178:179], v[18:19], off offset:3072
	global_load_dwordx2 v[180:181], v[68:69], off offset:3072
	global_load_dwordx2 v[182:183], v[76:77], off offset:3072
	global_load_dwordx2 v[184:185], v[92:93], off offset:3072
	global_load_dwordx4 v[200:203], v[96:97], off offset:2048
	s_nop 0
	v_pk_mul_f32 v[2:3], v[42:43], v[42:43]
	s_nop 0
	v_pk_fma_f32 v[2:3], v[58:59], v[58:59], v[2:3]
	s_nop 0
	v_pk_add_f32 v[62:63], v[2:3], v[2:3] op_sel:[0,1] op_sel_hi:[1,0]
	s_waitcnt vmcnt(19)
; __global__ void __launch_bounds__(NWAVES * 64, 2) trunk_fwd(Args args) {
;     ...
; #pragma unroll
;                     for (int jj = 0; jj < 8; ++jj) { const v2u a = y0[64 * jj], c = y1[64 * jj], a2 = z0[64 * jj], c2 = z1[64 * jj]; f32x4 x = xr[64 * jj];
;                         x.x += g0 * (bflo(a.x) + bflo(a2.x)) + g1 * (bflo(c.x) + bflo(c2.x)); x.y += g0 * (bfhi(a.x) + bfhi(a2.x)) + g1 * (bfhi(c.x) + bfhi(c2.x));
;                         x.z += g0 * (bflo(a.y) + bflo(a2.y)) + g1 * (bflo(c.y) + bflo(c2.y)); x.w += g0 * (bfhi(a.y) + bfhi(a2.y)) + g1 * (bfhi(c.y) + bfhi(c2.y));
;                         v[jj] = x; s += (x.x * x.x + x.y * x.y) + (x.z * x.z + x.w * x.w); }
	v_lshlrev_b32_e32 v6, 16, v204
	v_and_b32_e32 v7, 0xffff0000, v204
	s_waitcnt vmcnt(17)
	v_lshlrev_b32_e32 v22, 16, v208
	v_and_b32_e32 v23, 0xffff0000, v208
	v_pk_add_f32 v[6:7], v[6:7], v[22:23]
	v_lshlrev_b32_e32 v22, 16, v206
	v_and_b32_e32 v23, 0xffff0000, v206
	s_waitcnt vmcnt(16)
	v_lshlrev_b32_e32 v44, 16, v210
	v_and_b32_e32 v45, 0xffff0000, v210
	v_pk_add_f32 v[22:23], v[22:23], v[44:45]
	v_lshlrev_b32_e32 v204, 16, v211
	v_pk_mul_f32 v[22:23], v[94:95], v[22:23] op_sel_hi:[0,1]
	v_pk_fma_f32 v[6:7], v[52:53], v[6:7], v[22:23] op_sel_hi:[0,1,1]
	s_waitcnt vmcnt(15)
	v_pk_add_f32 v[44:45], v[212:213], v[6:7]
	v_lshlrev_b32_e32 v6, 16, v209
	v_mul_f32_e32 v212, v45, v45
	v_pk_fma_f32 v[82:83], v[44:45], v[44:45], v[212:213] op_sel_hi:[1,1,0]
	v_lshlrev_b32_e32 v212, 16, v205
	v_and_b32_e32 v213, 0xffff0000, v205
	v_and_b32_e32 v7, 0xffff0000, v209
	v_pk_add_f32 v[2:3], v[212:213], v[6:7]
	v_lshlrev_b32_e32 v6, 16, v207
	v_and_b32_e32 v7, 0xffff0000, v207
	v_and_b32_e32 v205, 0xffff0000, v211
	v_pk_add_f32 v[6:7], v[6:7], v[204:205]
	s_nop 0
	v_pk_mul_f32 v[6:7], v[94:95], v[6:7] op_sel_hi:[0,1]
	v_pk_fma_f32 v[2:3], v[52:53], v[2:3], v[6:7] op_sel_hi:[0,1,1]
	v_pk_add_f32 v[46:47], v[214:215], v[2:3]
	global_load_dwordx2 v[166:167], v[18:19], off offset:3584
	global_load_dwordx2 v[168:169], v[68:69], off offset:3584
	global_load_dwordx2 v[170:171], v[76:77], off offset:3584
	global_load_dwordx2 v[172:173], v[92:93], off offset:3584
	global_load_dwordx4 v[212:215], v[96:97], off offset:3072
	s_nop 0
	v_mul_f32_e32 v2, v47, v47
	v_pk_fma_f32 v[86:87], v[46:47], v[46:47], v[2:3] op_sel_hi:[1,1,0]
	s_waitcnt vmcnt(19)
	v_lshlrev_b32_e32 v206, 16, v217
	s_waitcnt vmcnt(18)
	v_lshlrev_b32_e32 v207, 16, v219
	s_waitcnt vmcnt(17)
	v_lshlrev_b32_e32 v208, 16, v221
	s_waitcnt vmcnt(16)
	v_lshlrev_b32_e32 v209, 16, v223
	v_pk_add_f32 v[78:79], v[206:207], v[208:209]
	v_and_b32_e32 v207, 0xffff0000, v219
	v_and_b32_e32 v206, 0xffff0000, v217
	v_and_b32_e32 v209, 0xffff0000, v223
	v_and_b32_e32 v208, 0xffff0000, v221
	v_pk_add_f32 v[88:89], v[206:207], v[208:209]
	v_lshlrev_b32_e32 v206, 16, v216
	v_and_b32_e32 v207, 0xffff0000, v216
	v_lshlrev_b32_e32 v216, 16, v220
	v_and_b32_e32 v217, 0xffff0000, v220
	v_lshlrev_b32_e32 v220, 16, v218
	v_and_b32_e32 v221, 0xffff0000, v218
	v_lshlrev_b32_e32 v218, 16, v222
	v_and_b32_e32 v219, 0xffff0000, v222
	v_pk_add_f32 v[4:5], v[220:221], v[218:219]
	v_pk_add_f32 v[2:3], v[206:207], v[216:217]
	v_pk_mul_f32 v[4:5], v[94:95], v[4:5] op_sel_hi:[0,1]
	v_pk_fma_f32 v[2:3], v[52:53], v[2:3], v[4:5] op_sel_hi:[0,1,1]
	s_waitcnt vmcnt(15)
	v_pk_add_f32 v[48:49], v[232:233], v[2:3]
	s_nop 0
	v_mul_f32_e32 v2, v49, v49
	v_pk_fma_f32 v[90:91], v[48:49], v[48:49], v[2:3] op_sel_hi:[1,1,0]
	s_waitcnt vmcnt(14)
	v_lshlrev_b32_e32 v232, 16, v236
	s_waitcnt vmcnt(13)
	v_lshlrev_b32_e32 v233, 16, v238
	s_waitcnt vmcnt(12)
	v_lshlrev_b32_e32 v50, 16, v240
	s_waitcnt vmcnt(11)
	v_lshlrev_b32_e32 v51, 16, v242
	v_pk_add_f32 v[20:21], v[232:233], v[50:51]
	v_and_b32_e32 v240, 0xffff0000, v240
	v_pk_mul_f32 v[20:21], v[52:53], v[20:21]
	v_and_b32_e32 v236, 0xffff0000, v236
	v_add_f32_e32 v20, v20, v21
	v_add_f32_e32 v236, v240, v236
	s_waitcnt vmcnt(10)
	v_add_f32_e32 v244, v244, v20
	v_mul_f32_e32 v20, v52, v236
	v_and_b32_e32 v236, 0xffff0000, v242
	v_and_b32_e32 v238, 0xffff0000, v238
	v_add_f32_e32 v236, v236, v238
	v_mul_f32_e32 v114, v53, v236
	v_lshlrev_b32_e32 v51, 16, v239
	v_lshlrev_b32_e32 v50, 16, v237
	v_lshlrev_b32_e32 v61, 16, v243
	v_lshlrev_b32_e32 v60, 16, v241
	v_and_b32_e32 v239, 0xffff0000, v239
	v_and_b32_e32 v238, 0xffff0000, v237
	v_and_b32_e32 v237, 0xffff0000, v243
	v_and_b32_e32 v236, 0xffff0000, v241
	v_pk_add_f32 v[50:51], v[50:51], v[60:61]
	v_pk_add_f32 v[2:3], v[238:239], v[236:237]
	v_pk_mul_f32 v[60:61], v[52:53], v[50:51]
	v_pk_mul_f32 v[50:51], v[52:53], v[2:3]
	v_mul_f32_e32 v80, v244, v244
	s_waitcnt vmcnt(9)
	v_lshlrev_b32_e32 v70, 16, v178
	s_waitcnt vmcnt(8)
	v_lshlrev_b32_e32 v71, 16, v180
	s_waitcnt vmcnt(7)
	v_lshlrev_b32_e32 v84, 16, v182
	s_waitcnt vmcnt(6)
	v_lshlrev_b32_e32 v85, 16, v184
	v_pk_add_f32 v[84:85], v[70:71], v[84:85]
	v_and_b32_e32 v71, 0xffff0000, v180
	v_and_b32_e32 v70, 0xffff0000, v178
	v_and_b32_e32 v117, 0xffff0000, v184
	v_and_b32_e32 v116, 0xffff0000, v182
	v_pk_add_f32 v[70:71], v[70:71], v[116:117]
	v_and_b32_e32 v180, 0xffff0000, v179
	v_pk_mul_f32 v[70:71], v[52:53], v[70:71]
	v_lshlrev_b32_e32 v117, 16, v185
	v_add_f32_e32 v178, v70, v71
	s_waitcnt vmcnt(5)
	v_add_f32_e32 v184, v201, v178
	v_lshlrev_b32_e32 v71, 16, v181
	v_lshlrev_b32_e32 v70, 16, v179
	v_and_b32_e32 v181, 0xffff0000, v181
	v_and_b32_e32 v179, 0xffff0000, v185
	v_and_b32_e32 v178, 0xffff0000, v183
	v_pk_add_f32 v[2:3], v[180:181], v[178:179]
	v_lshlrev_b32_e32 v116, 16, v183
	v_pk_mul_f32 v[2:3], v[52:53], v[2:3]
	v_pk_add_f32 v[70:71], v[70:71], v[116:117]
	v_add_f32_e32 v2, v2, v3
	v_add_f32_e32 v185, v203, v2
	s_nop 0
	s_nop 0
	s_nop 0
	v_mov_b32_e32 v92, v245
	v_mov_b32_e32 v182, v234
	v_mul_f32_e32 v234, v53, v79
	v_pk_fma_f32 v[78:79], v[52:53], v[78:79], v[234:235] op_sel_hi:[1,1,0]
	v_mul_f32_e32 v234, v53, v89
	v_mov_b32_e32 v93, v52
	v_mul_f32_e32 v74, v184, v184
	v_mul_f32_e32 v72, v185, v185
	s_waitcnt vmcnt(4)
	v_and_b32_e32 v21, 0xffff0000, v166
	s_waitcnt vmcnt(3)
	v_and_b32_e32 v201, 0xffff0000, v168
	s_waitcnt vmcnt(2)
	v_and_b32_e32 v115, 0xffff0000, v170
	s_waitcnt vmcnt(1)
; __global__ void __launch_bounds__(NWAVES * 64, 2) trunk_fwd(Args args) {
;     ...
;                     for (int jj = 0; jj < 8; ++jj) { const v2u a = y0[64 * jj], c = y1[64 * jj], a2 = z0[64 * jj], c2 = z1[64 * jj]; f32x4 x = xr[64 * jj];
;                         x.x += g0 * (bflo(a.x) + bflo(a2.x)) + g1 * (bflo(c.x) + bflo(c2.x)); x.y += g0 * (bfhi(a.x) + bfhi(a2.x)) + g1 * (bfhi(c.x) + bfhi(c2.x));
;                         x.z += g0 * (bflo(a.y) + bflo(a2.y)) + g1 * (bflo(c.y) + bflo(c2.y)); x.w += g0 * (bfhi(a.y) + bfhi(a2.y)) + g1 * (bfhi(c.y) + bfhi(c2.y));
;                         v[jj] = x; s += (x.x * x.x + x.y * x.y) + (x.z * x.z + x.w * x.w); }
;                     const float rstd = 1.0f / sqrtf(wave_sum(s) * (1.0f / D) + EPS);
	v_and_b32_e32 v245, 0xffff0000, v172
	v_add_f32_e32 v245, v245, v201
	v_mul_f32_e32 v97, v53, v245
	v_lshlrev_b32_e32 v245, 16, v167
	v_lshlrev_b32_e32 v201, 16, v171
	v_add_f32_e32 v245, v201, v245
	v_mul_f32_e32 v201, v52, v245
	v_lshlrev_b32_e32 v245, 16, v169
	v_lshlrev_b32_e32 v203, 16, v173
	v_add_f32_e32 v245, v203, v245
	v_pk_add_f32 v[20:21], v[20:21], v[114:115]
	v_mul_f32_e32 v114, v53, v245
	v_and_b32_e32 v245, 0xffff0000, v171
	v_and_b32_e32 v203, 0xffff0000, v167
	v_add_f32_e32 v245, v245, v203
	v_lshlrev_b32_e32 v183, 16, v166
	v_lshlrev_b32_e32 v95, 16, v168
	v_lshlrev_b32_e32 v81, 16, v172
	v_mul_f32_e32 v203, v52, v245
	v_and_b32_e32 v245, 0xffff0000, v173
	v_and_b32_e32 v166, 0xffff0000, v169
	v_lshlrev_b32_e32 v168, 16, v122
	v_and_b32_e32 v169, 0xffff0000, v122
	v_lshlrev_b32_e32 v172, 16, v158
	v_and_b32_e32 v173, 0xffff0000, v158
	v_pk_add_f32 v[116:117], v[168:169], v[172:173]
	v_lshlrev_b32_e32 v172, 16, v156
	v_and_b32_e32 v173, 0xffff0000, v156
	v_lshlrev_b32_e32 v156, 16, v157
	v_and_b32_e32 v157, 0xffff0000, v157
	v_pk_add_f32 v[118:119], v[172:173], v[120:121]
	v_pk_add_f32 v[100:101], v[156:157], v[160:161]
	v_lshlrev_b32_e32 v83, 16, v170
	v_pk_mul_f32 v[118:119], v[94:95], v[118:119] op_sel_hi:[0,1]
	v_pk_mul_f32 v[100:101], v[94:95], v[100:101] op_sel_hi:[0,1]
	v_mov_b32_e32 v94, v235
	v_pk_fma_f32 v[22:23], v[52:53], v[88:89], v[234:235] op_sel_hi:[1,1,0]
	v_lshlrev_b32_e32 v122, 16, v123
	v_and_b32_e32 v123, 0xffff0000, v123
	v_lshlrev_b32_e32 v158, 16, v159
	v_and_b32_e32 v159, 0xffff0000, v159
	v_mov_b32_e32 v79, v83
	v_mov_b32_e32 v23, v81
	v_pk_add_f32 v[104:105], v[122:123], v[158:159]
	v_pk_add_f32 v[78:79], v[182:183], v[78:79]
	v_pk_add_f32 v[88:89], v[94:95], v[22:23]
	v_pk_fma_f32 v[100:101], v[52:53], v[104:105], v[100:101] op_sel_hi:[0,1,1]
	v_mov_b32_e32 v182, v78
	v_mov_b32_e32 v183, v52
	v_mov_b32_e32 v22, v88
	v_mov_b32_e32 v23, v53
	v_pk_add_f32 v[68:69], v[92:93], v[20:21]
	v_pk_mul_f32 v[92:93], v[92:93], v[20:21]
	v_pk_add_f32 v[26:27], v[164:165], v[100:101]
	v_pk_mul_f32 v[100:101], v[182:183], v[78:79]
	v_pk_mul_f32 v[22:23], v[22:23], v[88:89]
	v_mov_b32_e32 v92, v68
	v_mov_b32_e32 v83, v101
	v_mov_b32_e32 v87, v23
	v_pk_fma_f32 v[22:23], v[182:183], v[78:79], v[22:23]
	s_waitcnt vmcnt(0)
	v_mov_b32_e32 v91, v212
	v_mov_b32_e32 v96, v68
	v_pk_add_f32 v[86:87], v[82:83], v[86:87]
	v_pk_add_f32 v[90:91], v[90:91], v[22:23]
	v_pk_mul_f32 v[22:23], v[68:69], v[68:69]
	v_pk_add_f32 v[82:83], v[92:93], v[96:97]
	v_mov_b32_e32 v81, v213
	v_mov_b32_e32 v23, v83
	v_pk_add_f32 v[22:23], v[80:81], v[22:23]
	v_mul_f32_e32 v80, v53, v85
	v_pk_fma_f32 v[80:81], v[52:53], v[84:85], v[80:81] op_sel_hi:[1,1,0]
	v_add_f32_e32 v245, v245, v166
	v_mov_b32_e32 v81, v114
	v_pk_add_f32 v[14:15], v[200:201], v[80:81]
	v_mov_b32_e32 v81, v214
	v_mul_f32_e32 v214, v53, v71
	v_mul_f32_e32 v245, v53, v245
	v_pk_fma_f32 v[116:117], v[52:53], v[116:117], v[118:119] op_sel_hi:[0,1,1]
	v_pk_fma_f32 v[52:53], v[52:53], v[70:71], v[214:215] op_sel_hi:[1,1,0]
	v_mov_b32_e32 v80, v14
	v_mov_b32_e32 v53, v245
	v_pk_add_f32 v[16:17], v[202:203], v[52:53]
	v_pk_add_f32 v[80:81], v[80:81], v[14:15]
	v_mov_b32_e32 v214, v16
	v_pk_add_f32 v[4:5], v[214:215], v[16:17]
	v_pk_fma_f32 v[52:53], v[14:15], v[14:15], v[74:75]
	v_pk_mul_f32 v[70:71], v[80:81], v[80:81]
	v_pk_mul_f32 v[84:85], v[4:5], v[4:5]
	v_mov_b32_e32 v53, v71
	v_pk_fma_f32 v[70:71], v[16:17], v[16:17], v[72:73]
	v_pk_add_f32 v[24:25], v[162:163], v[116:117]
	v_mov_b32_e32 v71, v85
	v_pk_add_f32 v[70:71], v[52:53], v[70:71]
	v_mov_b32_e32 v52, v64
	v_mov_b32_e32 v53, v66
	v_mov_b32_e32 v66, v65
	v_pk_add_f32 v[52:53], v[52:53], v[66:67]
	v_mov_b32_e32 v64, v25
	v_pk_add_f32 v[52:53], v[174:175], v[52:53]
	v_mov_b32_e32 v174, v24
	v_mov_b32_e32 v65, v53
	v_mov_b32_e32 v175, v52
	v_pk_mul_f32 v[64:65], v[64:65], v[64:65]
	v_pk_fma_f32 v[10:11], v[174:175], v[174:175], v[64:65]
	v_mov_b32_e32 v64, v54
	v_mov_b32_e32 v65, v56
	v_mov_b32_e32 v56, v55
	v_pk_add_f32 v[54:55], v[64:65], v[56:57]
	v_mov_b32_e32 v56, v27
	v_pk_add_f32 v[54:55], v[176:177], v[54:55]
	v_mov_b32_e32 v176, v26
	v_mov_b32_e32 v57, v55
	v_mov_b32_e32 v177, v54
	v_pk_mul_f32 v[56:57], v[56:57], v[56:57]
	v_lshl_add_u64 v[76:77], s[8:9], 0, v[186:187]
	v_pk_fma_f32 v[12:13], v[176:177], v[176:177], v[56:57]
	v_mov_b32_e32 v79, v88
	v_pk_add_f32 v[10:11], v[10:11], v[12:13]
	v_mov_b32_e32 v245, v68
	v_pk_add_f32 v[10:11], v[10:11], v[10:11] op_sel:[0,1] op_sel_hi:[1,0]
	s_add_u32 s8, s8, s38
	v_pk_add_f32 v[10:11], v[10:11], v[62:63]
	s_addc_u32 s9, s9, s39
	v_mov_b32_e32 v11, v212
	v_pk_add_f32 v[10:11], v[10:11], v[86:87]
	s_add_i32 s10, s10, s21
	v_pk_add_f32 v[56:57], v[10:11], v[90:91]
	v_pk_mul_f32 v[12:13], v[10:11], v[90:91]
	s_add_u32 s12, s12, s38
	v_mov_b32_e32 v57, v13
	v_mov_b32_e32 v12, v58
	v_mov_b32_e32 v13, v42
	v_mov_b32_e32 v42, v59
	v_mov_b32_e32 v58, v60
	v_mov_b32_e32 v59, v50
	v_mov_b32_e32 v50, v61
	v_pk_add_f32 v[50:51], v[58:59], v[50:51]
	s_addc_u32 s13, s13, s39
	v_pk_add_f32 v[8:9], v[246:247], v[50:51]
	s_cmpk_lt_i32 s7, 0x2000
	v_pk_mul_f32 v[50:51], v[8:9], v[8:9]
	s_nop 0
	v_mov_b32_e32 v212, v50
	v_mov_b32_e32 v82, v51
	v_pk_add_f32 v[2:3], v[212:213], v[82:83]
	s_nop 0
	v_pk_add_f32 v[50:51], v[22:23], v[2:3]
	v_pk_mul_f32 v[2:3], v[22:23], v[2:3]
	v_mov_b32_e32 v22, v11
	v_mov_b32_e32 v51, v3
	v_pk_add_f32 v[2:3], v[56:57], v[50:51]
	s_nop 0
	v_pk_add_f32 v[2:3], v[2:3], v[70:71]
	s_nop 0
	v_add_f32_e32 v2, v2, v3
	ds_bpermute_b32 v3, v73, v2
	s_waitcnt lgkmcnt(0)
; __global__ void __launch_bounds__(NWAVES * 64, 2) trunk_fwd(Args args) {
;     ...
;                     const float rstd = 1.0f / sqrtf(wave_sum(s) * (1.0f / D) + EPS);
;                     const f32x4* gr = (const f32x4*)args.in[I_NF] + lane; f32x4* orow = (f32x4*)(args.out + (size_t)m * D) + lane;
; #pragma unroll
;                     for (int jj = 0; jj < 8; ++jj) { const f32x4 gg = gr[64 * jj]; orow[64 * jj] = (f32x4){v[jj].x * rstd * gg.x, v[jj].y * rstd * gg.y, v[jj].z * rstd * gg.z, v[jj].w * rstd * gg.w}; }
	v_add_f32_e32 v2, v2, v3
	ds_bpermute_b32 v3, v75, v2
	s_waitcnt lgkmcnt(0)
	v_add_f32_e32 v2, v2, v3
	ds_bpermute_b32 v3, v108, v2
	s_waitcnt lgkmcnt(0)
	v_add_f32_e32 v2, v2, v3
	ds_bpermute_b32 v3, v109, v2
	s_waitcnt lgkmcnt(0)
	v_add_f32_e32 v2, v2, v3
	ds_bpermute_b32 v3, v110, v2
	s_waitcnt lgkmcnt(0)
	v_add_f32_e32 v2, v2, v3
	ds_bpermute_b32 v3, v111, v2
	s_waitcnt lgkmcnt(0)
	v_add_f32_e32 v2, v2, v3
	v_fmamk_f32 v2, v2, 0x3a000000, v226
	v_cmp_gt_f32_e32 vcc, s22, v2
	v_mul_f32_e32 v3, 0x4f800000, v2
	s_nop 0
	v_cndmask_b32_e32 v2, v2, v3, vcc
	v_sqrt_f32_e32 v3, v2
	s_nop 0
	v_add_u32_e32 v4, -1, v3
	v_fma_f32 v10, -v4, v3, v2
	v_cmp_ge_f32_e64 s[4:5], 0, v10
	v_add_u32_e32 v10, 1, v3
	s_nop 0
	v_cndmask_b32_e64 v4, v3, v4, s[4:5]
	v_fma_f32 v3, -v10, v3, v2
	v_cmp_lt_f32_e64 s[4:5], 0, v3
	s_nop 1
	v_cndmask_b32_e64 v3, v4, v10, s[4:5]
	v_mul_f32_e32 v4, 0x37800000, v3
	v_cndmask_b32_e32 v3, v3, v4, vcc
	v_cmp_class_f32_e32 vcc, v2, v225
	s_nop 1
	v_cndmask_b32_e32 v2, v3, v2, vcc
	v_div_scale_f32 v3, s[4:5], v2, v2, 1.0
	v_rcp_f32_e32 v4, v3
	s_nop 0
	v_fma_f32 v10, -v3, v4, 1.0
	v_fmac_f32_e32 v4, v10, v4
	v_div_scale_f32 v10, vcc, 1.0, v2, 1.0
	v_mul_f32_e32 v15, v10, v4
	v_fma_f32 v17, -v3, v15, v10
	v_fmac_f32_e32 v15, v17, v4
	v_fma_f32 v3, -v3, v15, v10
	v_div_fmas_f32 v3, v3, v4, v15
	v_div_fixup_f32 v10, v3, v2, 1.0
	v_pk_mul_f32 v[2:3], v[10:11], v[24:25] op_sel_hi:[0,1]
	v_pk_mul_f32 v[24:25], v[10:11], v[26:27] op_sel_hi:[0,1]
	v_pk_mul_f32 v[20:21], v[126:127], v[24:25]
	v_pk_mul_f32 v[18:19], v[124:125], v[2:3]
	global_store_dwordx4 v[76:77], v[18:21], off
	s_nop 1
	v_pk_mul_f32 v[2:3], v[10:11], v[54:55] op_sel_hi:[0,1]
	v_pk_mul_f32 v[24:25], v[10:11], v[52:53] op_sel_hi:[0,1]
	v_pk_mul_f32 v[6:7], v[10:11], v[244:245] op_sel_hi:[0,1]
	v_mov_b32_e32 v15, v184
	v_mov_b32_e32 v17, v185
	v_pk_mul_f32 v[14:15], v[10:11], v[14:15] op_sel_hi:[0,1]
	v_mov_b32_e32 v4, v81
	v_pk_mul_f32 v[4:5], v[10:11], v[4:5] op_sel_hi:[0,1]
	v_pk_mul_f32 v[18:19], v[128:129], v[24:25]
	v_pk_mul_f32 v[20:21], v[130:131], v[2:3]
	global_store_dwordx4 v[76:77], v[18:21], off offset:1024
	s_nop 1
	v_pk_mul_f32 v[2:3], v[10:11], v[12:13] op_sel_hi:[0,1]
	v_pk_mul_f32 v[12:13], v[10:11], v[44:45] op_sel_hi:[0,1]
	v_pk_mul_f32 v[18:19], v[132:133], v[2:3]
	v_pk_mul_f32 v[2:3], v[10:11], v[42:43] op_sel_hi:[0,1]
	v_pk_mul_f32 v[20:21], v[134:135], v[2:3]
	global_store_dwordx4 v[76:77], v[18:21], off offset:2048
	s_nop 1
	v_pk_mul_f32 v[2:3], v[10:11], v[46:47] op_sel_hi:[0,1]
	v_pk_mul_f32 v[18:19], v[136:137], v[12:13]
	v_pk_mul_f32 v[20:21], v[138:139], v[2:3]
	global_store_dwordx4 v[76:77], v[18:21], off offset:3072
	s_nop 1
	v_pk_mul_f32 v[2:3], v[10:11], v[48:49] op_sel_hi:[0,1]
	v_add_co_u32_e32 v12, vcc, s20, v76
	v_pk_mul_f32 v[18:19], v[140:141], v[2:3]
	v_pk_mul_f32 v[2:3], v[10:11], v[78:79] op_sel_hi:[0,1]
	v_pk_mul_f32 v[20:21], v[142:143], v[2:3]
	v_addc_co_u32_e32 v13, vcc, 0, v77, vcc
	global_store_dwordx4 v[12:13], v[18:21], off
	s_nop 1
	v_pk_mul_f32 v[2:3], v[10:11], v[8:9] op_sel_hi:[0,1]
	v_pk_mul_f32 v[6:7], v[144:145], v[6:7]
	v_pk_mul_f32 v[8:9], v[146:147], v[2:3]
	global_store_dwordx4 v[12:13], v[6:9], off offset:1024
	s_nop 1
	v_pk_mul_f32 v[2:3], v[10:11], v[16:17] op_sel_hi:[0,1]
	v_pk_mul_f32 v[6:7], v[148:149], v[14:15]
	v_pk_mul_f32 v[8:9], v[150:151], v[2:3]
	global_store_dwordx4 v[12:13], v[6:9], off offset:2048
	s_nop 1
	v_pk_mul_f32 v[2:3], v[10:11], v[22:23] op_sel_hi:[0,1]
	v_pk_mul_f32 v[2:3], v[152:153], v[2:3]
	v_pk_mul_f32 v[4:5], v[154:155], v[4:5]
	global_store_dwordx4 v[12:13], v[2:5], off offset:3072
	s_nop 1
	s_cbranch_scc1 .LBB0_1349
